# MoE-down epilogue: removed VALU instructions left dead by the lane-exchange store edit (old row addresses) and the never-read initialisations of the fp8 pack destinations
# baseline (speedup 1.0000x reference)
.LBB0_1352:
	s_mov_b32 s13, -1
	s_mov_b64 s[26:27], s[96:97]
	s_load_dwordx2 s[28:29], s[26:27], 0xd0
	v_mbcnt_lo_u32_b32 v0, s13, 0
	v_mbcnt_hi_u32_b32 v0, s13, v0
	v_lshrrev_b32_e32 v132, 1, v0
	v_ashrrev_i32_e32 v131, 31, v130
	s_waitcnt lgkmcnt(0)
	s_add_u32 s28, s28, s10
	s_addc_u32 s29, s29, s11
	s_lshl_b32 s13, s24, 8
	v_and_or_b32 v132, v132, 24, s13
	v_lshlrev_b64 v[130:131], 12, v[130:131]
	v_or_b32_e32 v138, s53, v132
	v_lshl_add_u64 v[130:131], s[28:29], 0, v[130:131]
	v_ashrrev_i32_e32 v139, 31, v138
	v_lshl_add_u64 v[142:143], v[138:139], 2, v[130:131]
	global_load_dwordx4 v[134:137], v[142:143], off
	global_load_dwordx4 v[130:133], v[142:143], off offset:16
	s_load_dwordx2 s[26:27], s[26:27], 0xe8
	v_and_or_b32 v0, v0, 15, s52
	v_lshl_add_u32 v172, s22, 8, v0
	s_waitcnt lgkmcnt(0)
	v_lshl_add_u64 v[158:159], s[26:27], 0, v[138:139]
	global_load_dwordx4 v[138:141], v[142:143], off offset:528
	s_nop 0
	global_load_dwordx4 v[142:145], v[142:143], off offset:512
	v_add_u32_e32 v174, 0x90, v172
	v_ashrrev_i32_e32 v175, 31, v174
	v_lshl_add_u64 v[178:179], v[158:159], 0, s[80:81]
	s_andn2_b64 vcc, exec, s[2:3]
	s_mov_b64 s[2:3], -1
	s_mov_b32 s68, s94
	s_waitcnt vmcnt(0)
	v_pk_fma_f32 v[86:87], v[86:87], s[86:87], v[134:135] op_sel_hi:[1,0,1]
	v_pk_fma_f32 v[90:91], v[90:91], s[86:87], v[130:131] op_sel_hi:[1,0,1]
	v_pk_fma_f32 v[78:79], v[78:79], s[86:87], v[134:135] op_sel_hi:[1,0,1]
	v_cvt_pk_fp8_f32 v157, v90, v91
	v_cvt_pk_fp8_f32 v90, v86, v87
	v_cvt_pk_fp8_f32 v86, v78, v79
	v_pk_fma_f32 v[58:59], v[58:59], s[86:87], v[130:131] op_sel_hi:[1,0,1]
	v_cvt_pk_fp8_f32 v79, v58, v59
	v_pk_fma_f32 v[66:67], v[66:67], s[86:87], v[134:135] op_sel_hi:[1,0,1]
	v_pk_fma_f32 v[60:61], v[60:61], s[86:87], v[132:133] op_sel_hi:[1,0,1]
	v_cvt_pk_fp8_f32 v78, v66, v67
	v_cvt_pk_fp8_f32 v79, v60, v61 op_sel:[0,0,1]
	v_pk_fma_f32 v[60:61], v[70:71], s[86:87], v[142:143] op_sel_hi:[1,0,1]
	v_cvt_pk_fp8_f32 v66, v60, v61
	v_pk_fma_f32 v[60:61], v[72:73], s[86:87], v[144:145] op_sel_hi:[1,0,1]
	v_pk_fma_f32 v[54:55], v[54:55], s[86:87], v[142:143] op_sel_hi:[1,0,1]
	v_pk_fma_f32 v[50:51], v[50:51], s[86:87], v[138:139] op_sel_hi:[1,0,1]
	v_cvt_pk_fp8_f32 v66, v60, v61 op_sel:[0,0,1]
	v_cvt_pk_fp8_f32 v60, v54, v55
	v_cvt_pk_fp8_f32 v61, v50, v51
	v_pk_fma_f32 v[50:51], v[56:57], s[86:87], v[144:145] op_sel_hi:[1,0,1]
	v_pk_fma_f32 v[46:47], v[46:47], s[86:87], v[142:143] op_sel_hi:[1,0,1]
	v_cvt_pk_fp8_f32 v60, v50, v51 op_sel:[0,0,1]
	v_cvt_pk_fp8_f32 v50, v46, v47
	v_pk_fma_f32 v[42:43], v[42:43], s[86:87], v[138:139] op_sel_hi:[1,0,1]
	v_cvt_pk_fp8_f32 v51, v42, v43
	v_pk_fma_f32 v[42:43], v[48:49], s[86:87], v[144:145] op_sel_hi:[1,0,1]
	v_pk_fma_f32 v[38:39], v[38:39], s[86:87], v[142:143] op_sel_hi:[1,0,1]
	v_cvt_pk_fp8_f32 v50, v42, v43 op_sel:[0,0,1]
	v_cvt_pk_fp8_f32 v42, v38, v39
	v_pk_fma_f32 v[34:35], v[34:35], s[86:87], v[138:139] op_sel_hi:[1,0,1]
	v_cvt_pk_fp8_f32 v43, v34, v35
	v_pk_fma_f32 v[34:35], v[40:41], s[86:87], v[144:145] op_sel_hi:[1,0,1]
	v_pk_fma_f32 v[30:31], v[30:31], s[86:87], v[142:143] op_sel_hi:[1,0,1]
	v_cvt_pk_fp8_f32 v42, v34, v35 op_sel:[0,0,1]
	v_cvt_pk_fp8_f32 v34, v30, v31
	v_pk_fma_f32 v[26:27], v[26:27], s[86:87], v[138:139] op_sel_hi:[1,0,1]
	v_cvt_pk_fp8_f32 v35, v26, v27
	v_pk_fma_f32 v[26:27], v[32:33], s[86:87], v[144:145] op_sel_hi:[1,0,1]
	v_pk_fma_f32 v[22:23], v[22:23], s[86:87], v[142:143] op_sel_hi:[1,0,1]
	v_cvt_pk_fp8_f32 v34, v26, v27 op_sel:[0,0,1]
	v_cvt_pk_fp8_f32 v26, v22, v23
	v_pk_fma_f32 v[18:19], v[18:19], s[86:87], v[138:139] op_sel_hi:[1,0,1]
	v_cvt_pk_fp8_f32 v27, v18, v19
	v_pk_fma_f32 v[18:19], v[24:25], s[86:87], v[144:145] op_sel_hi:[1,0,1]
	v_pk_fma_f32 v[14:15], v[14:15], s[86:87], v[142:143] op_sel_hi:[1,0,1]
	v_cvt_pk_fp8_f32 v26, v18, v19 op_sel:[0,0,1]
	v_cvt_pk_fp8_f32 v18, v14, v15
	v_pk_fma_f32 v[126:127], v[126:127], s[86:87], v[134:135] op_sel_hi:[1,0,1]
	v_pk_fma_f32 v[122:123], v[122:123], s[86:87], v[130:131] op_sel_hi:[1,0,1]
	v_pk_fma_f32 v[82:83], v[82:83], s[86:87], v[130:131] op_sel_hi:[1,0,1]
	v_pk_fma_f32 v[74:75], v[74:75], s[86:87], v[130:131] op_sel_hi:[1,0,1]
	v_pk_fma_f32 v[62:63], v[62:63], s[86:87], v[138:139] op_sel_hi:[1,0,1]
	v_pk_fma_f32 v[118:119], v[118:119], s[86:87], v[134:135] op_sel_hi:[1,0,1]
	v_pk_fma_f32 v[114:115], v[114:115], s[86:87], v[130:131] op_sel_hi:[1,0,1]
	v_cvt_pk_fp8_f32 v148, v126, v127
	v_cvt_pk_fp8_f32 v149, v122, v123
	v_cvt_pk_fp8_f32 v91, v82, v83
	v_cvt_pk_fp8_f32 v87, v74, v75
	v_cvt_pk_fp8_f32 v67, v62, v63
	v_pk_fma_f32 v[10:11], v[10:11], s[86:87], v[138:139] op_sel_hi:[1,0,1]
	v_pk_fma_f32 v[110:111], v[110:111], s[86:87], v[134:135] op_sel_hi:[1,0,1]
	v_pk_fma_f32 v[106:107], v[106:107], s[86:87], v[130:131] op_sel_hi:[1,0,1]
	v_cvt_pk_fp8_f32 v150, v118, v119
	v_cvt_pk_fp8_f32 v151, v114, v115
	v_cvt_pk_fp8_f32 v19, v10, v11
	v_pk_fma_f32 v[10:11], v[16:17], s[86:87], v[144:145] op_sel_hi:[1,0,1]
	v_pk_fma_f32 v[102:103], v[102:103], s[86:87], v[134:135] op_sel_hi:[1,0,1]
	v_pk_fma_f32 v[98:99], v[98:99], s[86:87], v[130:131] op_sel_hi:[1,0,1]
	v_cvt_pk_fp8_f32 v152, v110, v111
	v_cvt_pk_fp8_f32 v153, v106, v107
	v_cvt_pk_fp8_f32 v18, v10, v11 op_sel:[0,0,1]
	v_pk_fma_f32 v[6:7], v[6:7], s[86:87], v[142:143] op_sel_hi:[1,0,1]
	v_pk_fma_f32 v[2:3], v[2:3], s[86:87], v[138:139] op_sel_hi:[1,0,1]
	v_pk_fma_f32 v[128:129], v[128:129], s[86:87], v[136:137] op_sel_hi:[1,0,1]
	v_pk_fma_f32 v[124:125], v[124:125], s[86:87], v[132:133] op_sel_hi:[1,0,1]
	v_pk_fma_f32 v[94:95], v[94:95], s[86:87], v[134:135] op_sel_hi:[1,0,1]
	v_cvt_pk_fp8_f32 v154, v102, v103
	v_cvt_pk_fp8_f32 v155, v98, v99
	v_pk_fma_f32 v[82:83], v[88:89], s[86:87], v[136:137] op_sel_hi:[1,0,1]
	v_pk_fma_f32 v[84:85], v[84:85], s[86:87], v[132:133] op_sel_hi:[1,0,1]
	v_pk_fma_f32 v[74:75], v[80:81], s[86:87], v[136:137] op_sel_hi:[1,0,1]
	v_pk_fma_f32 v[76:77], v[76:77], s[86:87], v[132:133] op_sel_hi:[1,0,1]
	v_pk_fma_f32 v[58:59], v[68:69], s[86:87], v[136:137] op_sel_hi:[1,0,1]
	v_pk_fma_f32 v[62:63], v[64:65], s[86:87], v[140:141] op_sel_hi:[1,0,1]
	v_pk_fma_f32 v[28:29], v[28:29], s[86:87], v[140:141] op_sel_hi:[1,0,1]
	v_cvt_pk_fp8_f32 v10, v6, v7
	v_cvt_pk_fp8_f32 v11, v2, v3
	v_pk_fma_f32 v[120:121], v[120:121], s[86:87], v[136:137] op_sel_hi:[1,0,1]
	v_pk_fma_f32 v[116:117], v[116:117], s[86:87], v[132:133] op_sel_hi:[1,0,1]
	v_cvt_pk_fp8_f32 v156, v94, v95
	v_cvt_pk_fp8_f32 v148, v128, v129 op_sel:[0,0,1]
	v_cvt_pk_fp8_f32 v149, v124, v125 op_sel:[0,0,1]
	v_cvt_pk_fp8_f32 v90, v82, v83 op_sel:[0,0,1]
	v_cvt_pk_fp8_f32 v91, v84, v85 op_sel:[0,0,1]
	v_add_u32_e32 v84, 0xa0, v172
	v_cvt_pk_fp8_f32 v86, v74, v75 op_sel:[0,0,1]
	v_cvt_pk_fp8_f32 v87, v76, v77 op_sel:[0,0,1]
	v_add_u32_e32 v76, 0xb0, v172
	v_cvt_pk_fp8_f32 v78, v58, v59 op_sel:[0,0,1]
	v_cvt_pk_fp8_f32 v67, v62, v63 op_sel:[0,0,1]
	v_pk_fma_f32 v[52:53], v[52:53], s[86:87], v[140:141] op_sel_hi:[1,0,1]
	v_cvt_pk_fp8_f32 v35, v28, v29 op_sel:[0,0,1]
	v_pk_fma_f32 v[20:21], v[20:21], s[86:87], v[140:141] op_sel_hi:[1,0,1]
	v_pk_fma_f32 v[112:113], v[112:113], s[86:87], v[136:137] op_sel_hi:[1,0,1]
	v_pk_fma_f32 v[108:109], v[108:109], s[86:87], v[132:133] op_sel_hi:[1,0,1]
	v_cvt_pk_fp8_f32 v150, v120, v121 op_sel:[0,0,1]
	v_cvt_pk_fp8_f32 v151, v116, v117 op_sel:[0,0,1]
	v_ashrrev_i32_e32 v85, 31, v84
	v_ashrrev_i32_e32 v77, 31, v76
	v_cvt_pk_fp8_f32 v61, v52, v53 op_sel:[0,0,1]
	v_pk_fma_f32 v[44:45], v[44:45], s[86:87], v[140:141] op_sel_hi:[1,0,1]
	v_cvt_pk_fp8_f32 v27, v20, v21 op_sel:[0,0,1]
	v_pk_fma_f32 v[12:13], v[12:13], s[86:87], v[140:141] op_sel_hi:[1,0,1]
	v_pk_fma_f32 v[104:105], v[104:105], s[86:87], v[136:137] op_sel_hi:[1,0,1]
	v_pk_fma_f32 v[100:101], v[100:101], s[86:87], v[132:133] op_sel_hi:[1,0,1]
	v_cvt_pk_fp8_f32 v152, v112, v113 op_sel:[0,0,1]
	v_cvt_pk_fp8_f32 v153, v108, v109 op_sel:[0,0,1]
	v_lshlrev_b64 v[82:83], 10, v[174:175]
	v_lshlrev_b64 v[74:75], 10, v[84:85]
	v_lshlrev_b64 v[58:59], 10, v[76:77]
	v_cvt_pk_fp8_f32 v51, v44, v45 op_sel:[0,0,1]
	v_pk_fma_f32 v[36:37], v[36:37], s[86:87], v[140:141] op_sel_hi:[1,0,1]
	v_cvt_pk_fp8_f32 v19, v12, v13 op_sel:[0,0,1]
	v_pk_fma_f32 v[2:3], v[8:9], s[86:87], v[144:145] op_sel_hi:[1,0,1]
	v_pk_fma_f32 v[4:5], v[4:5], s[86:87], v[140:141] op_sel_hi:[1,0,1]
	v_pk_fma_f32 v[96:97], v[96:97], s[86:87], v[136:137] op_sel_hi:[1,0,1]
	v_pk_fma_f32 v[92:93], v[92:93], s[86:87], v[132:133] op_sel_hi:[1,0,1]
	v_cvt_pk_fp8_f32 v154, v104, v105 op_sel:[0,0,1]
	v_cvt_pk_fp8_f32 v155, v100, v101 op_sel:[0,0,1]
	v_lshl_add_u64 v[82:83], v[178:179], 0, v[82:83]
	v_lshl_add_u64 v[74:75], v[178:179], 0, v[74:75]
	v_lshl_add_u64 v[58:59], v[178:179], 0, v[58:59]
	v_cvt_pk_fp8_f32 v43, v36, v37 op_sel:[0,0,1]
	v_cvt_pk_fp8_f32 v10, v2, v3 op_sel:[0,0,1]
	v_cvt_pk_fp8_f32 v11, v4, v5 op_sel:[0,0,1]
	v_cvt_pk_fp8_f32 v156, v96, v97 op_sel:[0,0,1]
	v_cvt_pk_fp8_f32 v157, v92, v93 op_sel:[0,0,1]
	s_mov_b32 s98, -1
	v_mbcnt_lo_u32_b32 v180, s98, 0
	v_mbcnt_hi_u32_b32 v180, s98, v180
	v_and_b32_e32 v181, 3, v180
	v_lshrrev_b32_e32 v182, 2, v180
	v_lshlrev_b32_e32 v183, 4, v181
	v_or_b32_e32 v183, v183, v182
	v_lshlrev_b32_e32 v183, 2, v183
	ds_bpermute_b32 v148, v183, v148
	ds_bpermute_b32 v149, v183, v149
	ds_bpermute_b32 v150, v183, v150
	ds_bpermute_b32 v151, v183, v151
	ds_bpermute_b32 v152, v183, v152
	ds_bpermute_b32 v153, v183, v153
	ds_bpermute_b32 v154, v183, v154
	ds_bpermute_b32 v155, v183, v155
	ds_bpermute_b32 v156, v183, v156
	ds_bpermute_b32 v157, v183, v157
	ds_bpermute_b32 v90, v183, v90
	ds_bpermute_b32 v91, v183, v91
	ds_bpermute_b32 v86, v183, v86
	ds_bpermute_b32 v87, v183, v87
	ds_bpermute_b32 v78, v183, v78
	ds_bpermute_b32 v79, v183, v79
	ds_bpermute_b32 v66, v183, v66
	ds_bpermute_b32 v67, v183, v67
	ds_bpermute_b32 v60, v183, v60
	ds_bpermute_b32 v61, v183, v61
	ds_bpermute_b32 v50, v183, v50
	ds_bpermute_b32 v51, v183, v51
	ds_bpermute_b32 v42, v183, v42
	ds_bpermute_b32 v43, v183, v43
	ds_bpermute_b32 v34, v183, v34
	ds_bpermute_b32 v35, v183, v35
	ds_bpermute_b32 v26, v183, v26
	ds_bpermute_b32 v27, v183, v27
	ds_bpermute_b32 v18, v183, v18
	ds_bpermute_b32 v19, v183, v19
	ds_bpermute_b32 v10, v183, v10
	ds_bpermute_b32 v11, v183, v11
	v_lshlrev_b32_e32 v184, 3, v181
	v_or_b32_e32 v184, s13, v184
	v_or_b32_e32 v184, s53, v184
	v_mov_b32_e32 v185, 0
	v_lshl_add_u64 v[184:185], s[26:27], 0, v[184:185]
	v_lshl_add_u64 v[184:185], v[184:185], 0, s[80:81]
	v_or_b32_e32 v186, s52, v182
	v_lshl_add_u32 v186, s22, 8, v186
	v_lshlrev_b32_e32 v186, 10, v186
	v_mov_b32_e32 v187, 0
	v_lshl_add_u64 v[186:187], v[184:185], 0, v[186:187]
	s_mov_b32 s99, 0
	s_mov_b32 s98, 0x0
	v_lshl_add_u64 v[190:191], v[186:187], 0, s[98:99]
	s_mov_b32 s98, 0x4000
	v_lshl_add_u64 v[192:193], v[186:187], 0, s[98:99]
	s_mov_b32 s98, 0x8000
	v_lshl_add_u64 v[194:195], v[186:187], 0, s[98:99]
	s_mov_b32 s98, 0xc000
	v_lshl_add_u64 v[196:197], v[186:187], 0, s[98:99]
	s_mov_b32 s98, 0x20000
	v_lshl_add_u64 v[198:199], v[186:187], 0, s[98:99]
	s_mov_b32 s98, 0x24000
	v_lshl_add_u64 v[200:201], v[186:187], 0, s[98:99]
	s_mov_b32 s98, 0x28000
	v_lshl_add_u64 v[202:203], v[186:187], 0, s[98:99]
	s_mov_b32 s98, 0x2c000
	v_lshl_add_u64 v[204:205], v[186:187], 0, s[98:99]
	s_waitcnt lgkmcnt(0)
	global_store_dwordx2 v[190:191], v[148:149], off
	global_store_dwordx2 v[192:193], v[150:151], off
	global_store_dwordx2 v[194:195], v[152:153], off
	global_store_dwordx2 v[196:197], v[154:155], off
	global_store_dwordx2 v[198:199], v[156:157], off
	global_store_dwordx2 v[200:201], v[90:91], off
	global_store_dwordx2 v[202:203], v[86:87], off
	global_store_dwordx2 v[204:205], v[78:79], off
	global_store_dwordx2 v[190:191], v[66:67], off offset:128
	global_store_dwordx2 v[192:193], v[60:61], off offset:128
	global_store_dwordx2 v[194:195], v[50:51], off offset:128
	global_store_dwordx2 v[196:197], v[42:43], off offset:128
	global_store_dwordx2 v[198:199], v[34:35], off offset:128
	global_store_dwordx2 v[200:201], v[26:27], off offset:128
	global_store_dwordx2 v[202:203], v[18:19], off offset:128
	global_store_dwordx2 v[204:205], v[10:11], off offset:128
	s_cbranch_vccnz .LBB0_1341
	s_andn2_b64 vcc, exec, s[6:7]
	s_cbranch_vccnz .LBB0_1340
	s_barrier
	s_branch .LBB0_1340
